# helper share 7x171 runs (tuning after the attention and top-half loop fixes)
# baseline (speedup 1.0000x reference)
; #define LDS_AS __attribute__((address_space(3)))
; #define OPAQUE_TID(P) (((P).wid0 << 6) | lane_id_now())
; #define LAS __attribute__((address_space(3)))
; template <int NS, bool STREAM_ONLY = false>
; DI void convert_experts_dma(const Params& p, LDS_AS unsigned char* lds, int bid, int nb) {
;   const int tid = OPAQUE_TID(p), wid = __builtin_amdgcn_readfirstlane(tid >> 6), lane = tid & 63;
;   constexpr int NT = 32 * 1536;
;   const int nvalid = bid < NT / CVG ? CVG * ((NT / CVG - bid + nb - 1) / nb) : 0;
; __global__ void __launch_bounds__(NTHREADS, 2) k_forward(Params p_in) {
;     ...
;   if (is_cv) {
;     {
;       volatile LAS unsigned* stw = (volatile LAS unsigned*)dyn_smem;
;       const unsigned s0 = stw[0], s1 = stw[1];
;       __syncthreads();
;       convert_experts_dma<5>(p, (LDS_AS unsigned char*)dyn_smem, cvid, ncv);
.LBB0_1119:
	s_or_b64 exec, exec, s[0:1]
	s_mov_b64 s[12:13], 0
	s_mov_b32 s20, 0
	s_mov_b64 s[0:1], 0
	v_readlane_b32 s97, v255, 13
	s_mov_b32 s99, s96
	s_nop 0
	s_mov_b32 s98, s97
	s_cmp_lg_u32 s55, 0
	s_cbranch_scc0 .LBB0_1181
	v_readlane_b32 s98, v255, 17
	s_sub_i32 s99, s96, s55
	s_add_i32 s98, s98, 0x2b53
	s_branch .LBB0_1181
.LBB0_1121:
	v_mov_b32_e32 v0, 0
	ds_read_b32 v2, v0
	ds_read_b32 v3, v0 offset:4
	s_waitcnt lgkmcnt(0)
	s_barrier
	v_mbcnt_lo_u32_b32 v0, -1, 0
	v_mbcnt_hi_u32_b32 v0, -1, v0
	s_mov_b32 s6, 0
	v_or_b32_e32 v1, s87, v0
	s_cmpk_gt_i32 s54, 0x2b52
	v_readfirstlane_b32 s0, v1
	s_mov_b32 s18, 0
	s_cbranch_scc1 .LBB0_1123
	s_abs_i32 s1, s55
	v_cvt_f32_u32_e32 v1, s1
	s_sub_i32 s2, s55, s54
	s_add_i32 s3, s2, 0x2b52
	s_sub_i32 s2, 0xffffd4ae, s2
	v_rcp_iflag_f32_e32 v1, v1
	s_xor_b32 s5, s3, s55
	s_sub_i32 s4, 0, s1
	s_max_i32 s2, s3, s2
	v_mul_f32_e32 v1, 0x4f7ffffe, v1
	v_cvt_u32_f32_e32 v1, v1
	s_ashr_i32 s3, s5, 31
	v_readfirstlane_b32 s5, v1
	s_mul_i32 s4, s4, s5
	s_mul_hi_u32 s4, s5, s4
	s_add_i32 s5, s5, s4
	s_mul_hi_u32 s4, s2, s5
	s_mul_i32 s5, s4, s1
	s_sub_i32 s2, s2, s5
	s_add_i32 s7, s4, 1
	s_sub_i32 s5, s2, s1
	s_cmp_ge_u32 s2, s1
	s_cselect_b32 s4, s7, s4
	s_cselect_b32 s2, s5, s2
	s_add_i32 s5, s4, 1
	s_cmp_ge_u32 s2, s1
	s_cselect_b32 s1, s5, s4
	s_xor_b32 s1, s1, s3
	s_sub_i32 s1, s1, s3
	s_lshl_b32 s18, s1, 2
